# expert-weight conversion split: conversion workgroups take items [0,10240), the q-projection workgroups convert [10240,12288) after their cross-attention unit while waiting for the other half (s46/s47
# baseline (speedup 1.0000x reference)
; #define LAS __attribute__((address_space(3)))
; template <int PH, bool PRB = false>
; __device__ __forceinline__ void run_phase(int layer, LAS unsigned char* lds, const int wv_) {
;     ...
;     auto expert_cvt = [&](const int cb0, const int lo, const int hi) __attribute__((always_inline)) {
;         const int cgw = (bid - cb0) * (NT / 64) + wv, CNGW = (G - cb0) * (NT / 64); LAS float* scr = (LAS float*)(lds + wv * 16384);
;         const float* gf = p.ln_ffn + layer * D;
;         auto item_of = [&](int gi) __attribute__((always_inline)) {
;             const int e = gi / 768, r = gi % 768, m = r >> 8, j = r & 255; CvtItem it;
;             if (m < 2) { it.W = (m == 0 ? p.ewg : p.ewu) + ((size_t)layer * 16 + e) * D * 512; it.N = 512; it.K = D; it.g = gf; it.WT = MOE_FP8 ? (bf16*)((unsigned char*)wex + (size_t)e * WGU_SZ) : wex + e * WGU_SZ; it.k0 = 64 * (j >> 4); it.n0 = 32 * (j & 15); it.rowmode = 1 + m; it.fp8 = MOE_FP8; }
;             else { it.W = p.ewd + ((size_t)layer * 16 + e) * 512 * D; it.N = D; it.K = 512; it.g = nullptr; it.WT = wex + WEX_WD + e * WD_SZ; it.k0 = 64 * (j >> 5); it.n0 = 32 * (j & 31); it.rowmode = 0; }
;             return it; };
;         int gi = lo + cgw;
;         if (gi < hi) { CvtItem cur = item_of(gi); float v[32]; cvt_load(cur, v, lane);
;             for (;;) { const int gn = gi + CNGW; const bool more = gn < hi; CvtItem nxt = item_of(more ? gn : gi); float vn[32];
;                 if (more) cvt_load(nxt, vn, lane);
;                 cvt_finish(cur, v, scr, lane);
;                 if (!more) break;
; #pragma unroll
;                 for (int i = 0; i < 32; ++i) v[i] = vn[i];
;                 cur = nxt; gi = gn; } }
;     };
;     if constexpr (PH == PH_GEMM3) if (bid >= 128) expert_cvt(128, 0, CVT_PART1);
.LBB0_1002:
	s_mov_b32 s100, 0
.Lcv2_entry:
	s_mov_b32 s18, s80
	s_mov_b64 s[0:1], 0
	s_waitcnt lgkmcnt(0)
	v_readlane_b32 s2, v254, 1
	s_barrier
	v_readlane_b32 s3, v254, 2
	s_add_u32 s6, s2, s0
	s_addc_u32 s7, s3, s1
	s_load_dwordx2 s[16:17], s[6:7], 0xe0
	v_mbcnt_lo_u32_b32 v0, -1, 0
	v_mbcnt_hi_u32_b32 v0, -1, v0
	v_readlane_b32 s0, v254, 28
	v_add_u32_e32 v70, s93, v0
	v_readlane_b32 s34, v254, 0
	v_mov_b32_e32 v0, s0
	ds_read_b32 v0, v0
	s_cmpk_lt_i32 s34, 0x80
	s_waitcnt lgkmcnt(0)
	v_readfirstlane_b32 s42, v0
	s_cbranch_scc1 .Lcv2_chk
	s_lshl_b32 s0, s34, 3
	v_readlane_b32 s1, v254, 16
	s_add_i32 s33, s1, s0
	s_movk_i32 s101, 0x2800
	s_branch .Lcv2_go
.Lcv2_chk:
	s_cmp_eq_u32 s100, 0
	s_cbranch_scc1 .LBB0_1038
	s_lshl_b32 s0, s34, 3
	v_readlane_b32 s1, v254, 16
	s_add_i32 s33, s1, s0
	s_addk_i32 s33, 0x2c00
	s_movk_i32 s101, 0x3000
.Lcv2_go:
	s_cmp_ge_i32 s33, s101
	s_cbranch_scc1 .LBB0_1038
	s_load_dwordx2 s[0:1], s[6:7], 0x28
	s_load_dwordx2 s[4:5], s[6:7], 0xd0
	s_lshl_b32 s2, s18, 10
	s_ashr_i32 s3, s2, 31
	s_lshl_b64 s[2:3], s[2:3], 2
	s_waitcnt lgkmcnt(0)
	s_add_u32 s2, s0, s2
	s_addc_u32 s3, s1, s3
	s_add_u32 s35, s16, 0x1e400000
	s_mul_hi_i32 s0, s33, 0x2aaaaaab
	s_addc_u32 s36, s17, 0
	s_lshr_b32 s1, s0, 31
	s_ashr_i32 s0, s0, 7
	s_add_i32 s8, s0, s1
	s_mul_i32 s0, s8, 0x300
	s_sub_i32 s1, s33, s0
	s_ashr_i32 s26, s1, 8
	s_and_b32 s27, s1, 0xff
	s_cmp_gt_i32 s26, 1
	s_mov_b64 s[24:25], -1
	s_cbranch_scc0 .LBB0_1006
	s_ashr_i32 s19, s18, 31
	s_ashr_i32 s9, s8, 31
	s_lshl_b64 s[20:21], s[18:19], 25
	s_add_u32 s0, s4, s20
	s_addc_u32 s12, s5, s21
	s_lshl_b64 s[10:11], s[8:9], 21
	s_add_u32 s10, s0, s10
	s_addc_u32 s11, s12, s11
	s_lshl_b64 s[12:13], s[8:9], 20
	s_add_u32 s0, s16, s12
	s_addc_u32 s9, s17, s13
	s_add_u32 s22, s0, 0x20400000
	s_addc_u32 s23, s9, 0
	s_lshl_b32 s0, s27, 1
	s_lshl_b32 s9, s1, 5
	s_and_b32 s0, s0, 0x1c0
	s_and_b32 s50, s9, 0x3e0
	s_mov_b64 s[24:25], 0

; template <int PH, bool PRB = false>
; __device__ __forceinline__ void run_phase(int layer, LAS unsigned char* lds, const int wv_) {
;     ...
;             for (;;) { const int gn = gi + CNGW; const bool more = gn < hi; CvtItem nxt = item_of(more ? gn : gi); float vn[32];
;                 if (more) cvt_load(nxt, vn, lane);
;                 cvt_finish(cur, v, scr, lane);
;                 if (!more) break;
; #pragma unroll
;                 for (int i = 0; i < 32; ++i) v[i] = vn[i];
;                 cur = nxt; gi = gn; } }
.Lcv_nog:
	s_add_i32 s6, s90, s33
	s_add_i32 s10, s6, 0xfffffc00
	s_cmp_lt_i32 s10, s101
	s_cselect_b64 s[30:31], -1, 0
	s_and_b64 s[6:7], s[30:31], exec
	s_cselect_b32 s7, s10, s33
	s_mul_hi_i32 s6, s7, 0x2aaaaaab
	s_lshr_b32 s10, s6, 31
	s_ashr_i32 s6, s6, 7
	s_add_i32 s6, s6, s10
	s_mul_i32 s10, s6, 0x300
	s_sub_i32 s27, s7, s10
	s_ashr_i32 s26, s27, 8
	s_and_b32 s43, s27, 0xff
	s_cmp_gt_i32 s26, 1
	s_mov_b64 s[10:11], -1
	s_cbranch_scc0 .LBB0_1013
	s_ashr_i32 s7, s6, 31
	s_lshl_b64 s[10:11], s[6:7], 21
	s_add_u32 s28, s37, s10
	s_addc_u32 s29, s38, s11
	s_lshl_b64 s[10:11], s[6:7], 20
	s_add_u32 s24, s39, s10
	s_addc_u32 s25, s40, s11
	s_lshl_b32 s7, s43, 1
	s_and_b32 s41, s7, 0x1c0
	s_lshl_b32 s7, s27, 5
	s_and_b32 s50, s7, 0x3e0
	s_mov_b64 s[10:11], 0

; template <int PH, bool PRB = false>
; __device__ __forceinline__ void run_phase(int layer, LAS unsigned char* lds, const int wv_) {
;     ...
;     if constexpr (PH == PH_GEMM3) if (bid < 128) {
;         pg8::DenseSched Sd; Sd.init(S, 512, D, wnx + WO_WQ + layer * WQ_SZ, 128, bid);
;         pg8::Unit u0; Sd.next(0, u0);
;         pg8::wait_counter(ctl + CW_G2 + layer * 4096 + 64 * u0.pm, 32u, xtmo, wv);
.LBB0_1038:
	s_cmp_lg_u32 s100, 0
	s_cbranch_scc1 .Lcv2_ret
	s_cmpk_gt_i32 s34, 0x7f
	s_cbranch_scc1 .LBB0_1182
	s_ashr_i32 s0, s34, 31
	s_lshr_b32 s0, s0, 29
	s_add_i32 s4, s34, s0
	s_and_b32 s0, s4, -8
	s_sub_i32 s11, s34, s0
	s_cmp_gt_i32 s11, -1
	s_cselect_b64 s[0:1], -1, 0
	s_mov_b64 s[2:3], -1
	s_and_b64 vcc, exec, s[0:1]
	s_cbranch_vccz .LBB0_1041
	s_lshl_b32 s5, s11, 4
	s_mov_b64 s[2:3], 0

; template <int PH, bool PRB = false>
; __device__ __forceinline__ void run_phase(int layer, LAS unsigned char* lds, const int wv_) {
;     ...
;     if constexpr (PH == PH_GEMM4) {
;         pg8::DenseSched Sd; Sd.init(S, D, 512, wnx + WO_WO + layer * WO_SZ, G, bid); Sd.wready = oready; Sd.wneed = 32u; Sd.wtmo = xtmo;
;         pg8::EpiResidual<false, true, PRB> E{nullptr, hb, ssqp, PRB ? ctl + 258048 : hready}; E.wt = wtf;
;         pg8::gemm_phase(lds, ox, 512, Sd, E, wv);
.LBB0_1243:
	s_or_b64 exec, exec, s[0:1]
	s_mov_b32 s0, s80
	s_mov_b64 s[2:3], 0
	s_barrier
	v_readlane_b32 s34, v254, 0
	s_nop 0
	s_cmpk_lt_i32 s34, 0x80
	s_cbranch_scc0 .Lcv2_done
	s_mov_b32 s100, 1
	s_mov_b32 s48, s46
	s_mov_b32 s49, s47
	s_branch .Lcv2_entry
.Lcv2_ret:
	s_waitcnt vmcnt(0)
	s_mov_b32 s100, 0
	s_mov_b32 s46, s48
	s_mov_b32 s47, s49
.Lcv2_done:
	s_mov_b32 s0, s80
	s_mov_b64 s[2:3], 0
	s_barrier
	v_readlane_b32 s4, v254, 1
	v_readlane_b32 s5, v254, 2
	s_add_u32 s2, s4, s2
	s_addc_u32 s3, s5, s3
	s_load_dwordx2 s[2:3], s[2:3], 0xe0
	v_mbcnt_lo_u32_b32 v0, -1, 0
	v_mbcnt_hi_u32_b32 v0, -1, v0
	v_readlane_b32 s1, v254, 28
	v_add_u32_e32 v0, s93, v0
	v_readlane_b32 s33, v254, 0
	v_mov_b32_e32 v0, s1
	ds_read_b32 v0, v0
	s_cmpk_lt_i32 s33, 0x100
	s_cselect_b64 s[4:5], -1, 0
	s_cmpk_gt_i32 s33, 0xff
	s_waitcnt lgkmcnt(0)
	v_readfirstlane_b32 s16, v0
	v_mbcnt_lo_u32_b32 v0, -1, 0
	v_mbcnt_hi_u32_b32 v0, -1, v0
	s_nop 0
	v_add_u32_e32 v6, s93, v0
	s_nop 0
	v_readfirstlane_b32 s18, v6
	s_cbranch_scc1 .LBB0_1249
	s_ashr_i32 s1, s33, 31
	s_lshr_b32 s1, s1, 29
	s_add_i32 s1, s33, s1
	s_and_b32 s6, s1, -8
	s_sub_i32 s8, s33, s6
	s_cmp_gt_i32 s8, -1
	s_mov_b64 s[6:7], -1
	s_cbranch_scc0 .LBB0_1246
	s_lshl_b32 s9, s8, 5
	s_mov_b64 s[6:7], 0
